# code prefetch also in k_prep/k_final (with 256B end padding of .text) and k_layer<2> prefetch range extended to its full 14.7 KB
# speedup vs baseline: 1.3681x; 1.0070x over previous
_Z6k_prepPKiS0_PKfS2_S2_S2_S2_S2_S2_S2_S2_S2_PDF16_S3_S3_PfS4_S4_PjS3_S5_:
	s_getpc_b64 s[4:5]
	v_lshlrev_b32_e32 v61, 6, v0
	s_movk_i32 s6, 0x28
	v_cmp_gt_u32_e32 vcc, s6, v0
	s_and_saveexec_b64 s[6:7], vcc
	global_load_dword v61, v61, s[4:5]
	s_mov_b64 exec, s[6:7]
	v_lshl_or_b32 v2, s2, 10, v0
	s_mov_b32 s2, 0xffff7f7f
	v_add_u32_e32 v14, 0x10080, v2
	v_cmp_lt_i32_e32 vcc, s2, v2
	s_and_saveexec_b64 s[2:3], vcc
	s_xor_b64 s[8:9], exec, s[2:3]
	s_cbranch_execnz .LBB0_3
	s_andn2_saveexec_b64 s[2:3], s[8:9]
	s_cbranch_execnz .LBB0_32

	.amdhsa_kernel _Z6k_prepPKiS0_PKfS2_S2_S2_S2_S2_S2_S2_S2_S2_PDF16_S3_S3_PfS4_S4_PjS3_S5_
		.amdhsa_group_segment_fixed_size 0
		.amdhsa_private_segment_fixed_size 0
		.amdhsa_kernarg_size 168
		.amdhsa_user_sgpr_count 2
		.amdhsa_user_sgpr_dispatch_ptr 0
		.amdhsa_user_sgpr_queue_ptr 0
		.amdhsa_user_sgpr_kernarg_segment_ptr 1
		.amdhsa_user_sgpr_dispatch_id 0
		.amdhsa_user_sgpr_kernarg_preload_length 0
		.amdhsa_user_sgpr_kernarg_preload_offset 0
		.amdhsa_user_sgpr_private_segment_size 0
		.amdhsa_uses_dynamic_stack 0
		.amdhsa_enable_private_segment 0
		.amdhsa_system_sgpr_workgroup_id_x 1
		.amdhsa_system_sgpr_workgroup_id_y 0
		.amdhsa_system_sgpr_workgroup_id_z 0
		.amdhsa_system_sgpr_workgroup_info 0
		.amdhsa_system_vgpr_workitem_id 0
		.amdhsa_next_free_vgpr 62
		.amdhsa_next_free_sgpr 21
		.amdhsa_accum_offset 64
		.amdhsa_reserve_vcc 1
		.amdhsa_float_round_mode_32 0
		.amdhsa_float_round_mode_16_64 0
		.amdhsa_float_denorm_mode_32 3
		.amdhsa_float_denorm_mode_16_64 3
		.amdhsa_dx10_clamp 1
		.amdhsa_ieee_mode 1
		.amdhsa_fp16_overflow 0
		.amdhsa_tg_split 0
		.amdhsa_exception_fp_ieee_invalid_op 0
		.amdhsa_exception_fp_denorm_src 0
		.amdhsa_exception_fp_ieee_div_zero 0
		.amdhsa_exception_fp_ieee_overflow 0
		.amdhsa_exception_fp_ieee_underflow 0
		.amdhsa_exception_fp_ieee_inexact 0
		.amdhsa_exception_int_div_zero 0
	.end_amdhsa_kernel

_Z7k_finalPKfS0_Pf:
	s_getpc_b64 s[4:5]
	v_lshlrev_b32_e32 v10, 6, v0
	s_movk_i32 s6, 0x8
	v_cmp_gt_u32_e32 vcc, s6, v0
	s_and_saveexec_b64 s[6:7], vcc
	global_load_dword v10, v10, s[4:5]
	s_mov_b64 exec, s[6:7]
	v_lshl_or_b32 v2, s2, 8, v0
	s_movk_i32 s2, 0x7d0
	v_cmp_gt_i32_e32 vcc, s2, v2
	s_and_saveexec_b64 s[2:3], vcc
	s_cbranch_execz .LBB3_2
	s_load_dwordx4 s[4:7], s[0:1], 0x0
	s_load_dwordx2 s[2:3], s[0:1], 0x10
	v_lshlrev_b32_e32 v4, 1, v2
	v_and_b32_e32 v3, 1, v0
	v_or_b32_e32 v0, 2, v4
	v_ashrrev_i32_e32 v1, 31, v0
	s_waitcnt lgkmcnt(0)
	v_lshl_add_u64 v[0:1], v[0:1], 2, s[4:5]
	global_load_dword v5, v[0:1], off
	v_and_or_b32 v0, v4, -4, v3
	v_ashrrev_i32_e32 v1, 31, v0
	v_lshl_add_u64 v[0:1], v[0:1], 2, s[4:5]
	global_load_dword v0, v[0:1], off
	v_lshlrev_b32_e32 v1, 2, v3
	global_load_dword v1, v1, s[6:7]
	s_waitcnt vmcnt(2)
	v_max_f32_e32 v3, v5, v5
	v_max_f32_e32 v4, 1.0, v3
	v_ashrrev_i32_e32 v3, 31, v2
	s_waitcnt vmcnt(1)
	v_div_scale_f32 v5, s[0:1], v4, v4, v0
	v_rcp_f32_e32 v6, v5
	v_div_scale_f32 v7, vcc, v0, v4, v0
	v_fma_f32 v8, -v5, v6, 1.0
	v_fmac_f32_e32 v6, v8, v6
	v_mul_f32_e32 v8, v7, v6
	v_fma_f32 v9, -v5, v8, v7
	v_fmac_f32_e32 v8, v9, v6
	v_fma_f32 v5, -v5, v8, v7
	v_div_fmas_f32 v5, v5, v6, v8
	v_div_fixup_f32 v0, v5, v4, v0
	s_waitcnt vmcnt(0)
	v_add_f32_e32 v4, v0, v1
	v_lshl_add_u64 v[0:1], v[2:3], 2, s[2:3]
	global_store_dword v[0:1], v4, off

	.amdhsa_kernel _Z7k_finalPKfS0_Pf
		.amdhsa_group_segment_fixed_size 0
		.amdhsa_private_segment_fixed_size 0
		.amdhsa_kernarg_size 24
		.amdhsa_user_sgpr_count 2
		.amdhsa_user_sgpr_dispatch_ptr 0
		.amdhsa_user_sgpr_queue_ptr 0
		.amdhsa_user_sgpr_kernarg_segment_ptr 1
		.amdhsa_user_sgpr_dispatch_id 0
		.amdhsa_user_sgpr_kernarg_preload_length 0
		.amdhsa_user_sgpr_kernarg_preload_offset 0
		.amdhsa_user_sgpr_private_segment_size 0
		.amdhsa_uses_dynamic_stack 0
		.amdhsa_enable_private_segment 0
		.amdhsa_system_sgpr_workgroup_id_x 1
		.amdhsa_system_sgpr_workgroup_id_y 0
		.amdhsa_system_sgpr_workgroup_id_z 0
		.amdhsa_system_sgpr_workgroup_info 0
		.amdhsa_system_vgpr_workitem_id 0
		.amdhsa_next_free_vgpr 11
		.amdhsa_next_free_sgpr 8
		.amdhsa_accum_offset 12
		.amdhsa_reserve_vcc 1
		.amdhsa_float_round_mode_32 0
		.amdhsa_float_round_mode_16_64 0
		.amdhsa_float_denorm_mode_32 3
		.amdhsa_float_denorm_mode_16_64 3
		.amdhsa_dx10_clamp 1
		.amdhsa_ieee_mode 1
		.amdhsa_fp16_overflow 0
		.amdhsa_tg_split 0
		.amdhsa_exception_fp_ieee_invalid_op 0
		.amdhsa_exception_fp_denorm_src 0
		.amdhsa_exception_fp_ieee_div_zero 0
		.amdhsa_exception_fp_ieee_overflow 0
		.amdhsa_exception_fp_ieee_underflow 0
		.amdhsa_exception_fp_ieee_inexact 0
		.amdhsa_exception_int_div_zero 0
	.end_amdhsa_kernel

_Z7k_layerILi2EEvPKDF16_PKiPKjS3_S3_S1_PKfPDF16_PhS3_S7_Pf:
	s_getpc_b64 s[4:5]
	v_lshlrev_b32_e32 v104, 6, v0
	s_movk_i32 s6, 0xe5
	v_cmp_gt_u32_e32 vcc, s6, v0
	s_and_saveexec_b64 s[6:7], vcc
	global_load_dword v104, v104, s[4:5]
	s_mov_b64 exec, s[6:7]
	v_readfirstlane_b32 s3, v0
	s_lshr_b32 s3, s3, 6
	s_cmp_eq_u32 s3, 0
	s_cbranch_scc1 .Lic2p_t0
	s_cmp_eq_u32 s3, 1
	s_cbranch_scc1 .Lic2p_t1
	s_cmp_eq_u32 s3, 2
	s_cbranch_scc1 .Lic2p_t2
	s_cmp_eq_u32 s3, 3
	s_cbranch_scc1 .Lic2p_t3
	s_cmp_eq_u32 s3, 4
	s_cbranch_scc1 .Lic2p_t4
	s_cmp_eq_u32 s3, 5
	s_cbranch_scc1 .Lic2p_t5
	s_cmp_eq_u32 s3, 6
	s_cbranch_scc1 .Lic2p_t6
	s_cmp_eq_u32 s3, 7
	s_cbranch_scc1 .Lic2p_t7
	s_cmp_eq_u32 s3, 8
	s_cbranch_scc1 .Lic2p_t8
	s_cmp_eq_u32 s3, 9
	s_cbranch_scc1 .Lic2p_t9

amdhsa.kernels:
  - .agpr_count:     0
    .args:
      - .actual_access:  read_only
        .address_space:  global
        .offset:         0
        .size:           8
        .value_kind:     global_buffer
      - .actual_access:  read_only
        .address_space:  global
        .offset:         8
        .size:           8
        .value_kind:     global_buffer
      - .actual_access:  read_only
        .address_space:  global
        .offset:         16
        .size:           8
        .value_kind:     global_buffer
      - .actual_access:  read_only
        .address_space:  global
        .offset:         24
        .size:           8
        .value_kind:     global_buffer
      - .actual_access:  read_only
        .address_space:  global
        .offset:         32
        .size:           8
        .value_kind:     global_buffer
      - .actual_access:  read_only
        .address_space:  global
        .offset:         40
        .size:           8
        .value_kind:     global_buffer
      - .actual_access:  read_only
        .address_space:  global
        .offset:         48
        .size:           8
        .value_kind:     global_buffer
      - .actual_access:  read_only
        .address_space:  global
        .offset:         56
        .size:           8
        .value_kind:     global_buffer
      - .actual_access:  read_only
        .address_space:  global
        .offset:         64
        .size:           8
        .value_kind:     global_buffer
      - .actual_access:  read_only
        .address_space:  global
        .offset:         72
        .size:           8
        .value_kind:     global_buffer
      - .actual_access:  read_only
        .address_space:  global
        .offset:         80
        .size:           8
        .value_kind:     global_buffer
      - .actual_access:  read_only
        .address_space:  global
        .offset:         88
        .size:           8
        .value_kind:     global_buffer
      - .actual_access:  write_only
        .address_space:  global
        .offset:         96
        .size:           8
        .value_kind:     global_buffer
      - .actual_access:  write_only
        .address_space:  global
        .offset:         104
        .size:           8
        .value_kind:     global_buffer
      - .actual_access:  write_only
        .address_space:  global
        .offset:         112
        .size:           8
        .value_kind:     global_buffer
      - .actual_access:  write_only
        .address_space:  global
        .offset:         120
        .size:           8
        .value_kind:     global_buffer
      - .actual_access:  write_only
        .address_space:  global
        .offset:         128
        .size:           8
        .value_kind:     global_buffer
      - .actual_access:  write_only
        .address_space:  global
        .offset:         136
        .size:           8
        .value_kind:     global_buffer
      - .actual_access:  write_only
        .address_space:  global
        .offset:         144
        .size:           8
        .value_kind:     global_buffer
      - .actual_access:  write_only
        .address_space:  global
        .offset:         152
        .size:           8
        .value_kind:     global_buffer
      - .actual_access:  write_only
        .address_space:  global
        .offset:         160
        .size:           8
        .value_kind:     global_buffer
    .group_segment_fixed_size: 0
    .kernarg_segment_align: 8
    .kernarg_segment_size: 168
    .language:       OpenCL C
    .language_version:
      - 2
      - 0
    .max_flat_workgroup_size: 1024
    .name:           _Z6k_prepPKiS0_PKfS2_S2_S2_S2_S2_S2_S2_S2_S2_PDF16_S3_S3_PfS4_S4_PjS3_S5_
    .private_segment_fixed_size: 0
    .sgpr_count:     27
    .sgpr_spill_count: 0
    .symbol:         _Z6k_prepPKiS0_PKfS2_S2_S2_S2_S2_S2_S2_S2_S2_PDF16_S3_S3_PfS4_S4_PjS3_S5_.kd
    .uniform_work_group_size: 1
    .uses_dynamic_stack: false
    .vgpr_count:     62
    .vgpr_spill_count: 0
    .wavefront_size: 64
  - .agpr_count:     0
    .args:
      - .actual_access:  read_only
        .address_space:  global
        .offset:         0
        .size:           8
        .value_kind:     global_buffer
      - .actual_access:  read_only
        .address_space:  global
        .offset:         8
        .size:           8
        .value_kind:     global_buffer
      - .actual_access:  read_only
        .address_space:  global
        .offset:         16
        .size:           8
        .value_kind:     global_buffer
      - .actual_access:  write_only
        .address_space:  global
        .offset:         24
        .size:           8
        .value_kind:     global_buffer
      - .actual_access:  write_only
        .address_space:  global
        .offset:         32
        .size:           8
        .value_kind:     global_buffer
      - .actual_access:  write_only
        .address_space:  global
        .offset:         40
        .size:           8
        .value_kind:     global_buffer
      - .actual_access:  read_only
        .address_space:  global
        .offset:         48
        .size:           8
        .value_kind:     global_buffer
      - .actual_access:  read_only
        .address_space:  global
        .offset:         56
        .size:           8
        .value_kind:     global_buffer
      - .actual_access:  read_only
        .address_space:  global
        .offset:         64
        .size:           8
        .value_kind:     global_buffer
      - .actual_access:  read_only
        .address_space:  global
        .offset:         72
        .size:           8
        .value_kind:     global_buffer
      - .actual_access:  read_only
        .address_space:  global
        .offset:         80
        .size:           8
        .value_kind:     global_buffer
      - .actual_access:  read_only
        .address_space:  global
        .offset:         88
        .size:           8
        .value_kind:     global_buffer
      - .actual_access:  read_only
        .address_space:  global
        .offset:         96
        .size:           8
        .value_kind:     global_buffer
      - .actual_access:  read_only
        .address_space:  global
        .offset:         104
        .size:           8
        .value_kind:     global_buffer
      - .actual_access:  read_only
        .address_space:  global
        .offset:         112
        .size:           8
        .value_kind:     global_buffer
      - .actual_access:  read_only
        .address_space:  global
        .offset:         120
        .size:           8
        .value_kind:     global_buffer
      - .actual_access:  read_only
        .address_space:  global
        .offset:         128
        .size:           8
        .value_kind:     global_buffer
      - .actual_access:  write_only
        .address_space:  global
        .offset:         136
        .size:           8
        .value_kind:     global_buffer
      - .actual_access:  write_only
        .address_space:  global
        .offset:         144
        .size:           8
        .value_kind:     global_buffer
      - .actual_access:  write_only
        .address_space:  global
        .offset:         152
        .size:           8
        .value_kind:     global_buffer
      - .actual_access:  write_only
        .address_space:  global
        .offset:         160
        .size:           8
        .value_kind:     global_buffer
      - .actual_access:  write_only
        .address_space:  global
        .offset:         168
        .size:           8
        .value_kind:     global_buffer
    .group_segment_fixed_size: 1696
    .kernarg_segment_align: 8
    .kernarg_segment_size: 176
    .language:       OpenCL C
    .language_version:
      - 2
      - 0
    .max_flat_workgroup_size: 1024
    .name:           _Z11k_localsortPKiS0_S0_PjPtPiPKjPKfS7_S7_S7_S7_S7_S7_S7_S7_S7_PDF16_S8_S8_PfS9_
    .private_segment_fixed_size: 0
    .sgpr_count:     71
    .sgpr_spill_count: 0
    .symbol:         _Z11k_localsortPKiS0_S0_PjPtPiPKjPKfS7_S7_S7_S7_S7_S7_S7_S7_S7_PDF16_S8_S8_PfS9_.kd
    .uniform_work_group_size: 1
    .uses_dynamic_stack: false
    .vgpr_count:     96
    .vgpr_spill_count: 0
    .wavefront_size: 64
  - .agpr_count:     0
    .args:
      - .actual_access:  read_only
        .address_space:  global
        .offset:         0
        .size:           8
        .value_kind:     global_buffer
      - .actual_access:  read_only
        .address_space:  global
        .offset:         8
        .size:           8
        .value_kind:     global_buffer
      - .actual_access:  read_only
        .address_space:  global
        .offset:         16
        .size:           8
        .value_kind:     global_buffer
      - .actual_access:  write_only
        .address_space:  global
        .offset:         24
        .size:           8
        .value_kind:     global_buffer
      - .actual_access:  write_only
        .address_space:  global
        .offset:         32
        .size:           8
        .value_kind:     global_buffer
    .group_segment_fixed_size: 54160
    .kernarg_segment_align: 8
    .kernarg_segment_size: 40
    .language:       OpenCL C
    .language_version:
      - 2
      - 0
    .max_flat_workgroup_size: 1024
    .name:           _Z12k_bucketsortPKjPKtPKiPiPj
    .private_segment_fixed_size: 0
    .sgpr_count:     88
    .sgpr_spill_count: 0
    .symbol:         _Z12k_bucketsortPKjPKtPKiPiPj.kd
    .uniform_work_group_size: 1
    .uses_dynamic_stack: false
    .vgpr_count:     64
    .vgpr_spill_count: 0
    .wavefront_size: 64
  - .agpr_count:     0
    .args:
      - .actual_access:  read_only
        .address_space:  global
        .offset:         0
        .size:           8
        .value_kind:     global_buffer
      - .actual_access:  read_only
        .address_space:  global
        .offset:         8
        .size:           8
        .value_kind:     global_buffer
      - .actual_access:  write_only
        .address_space:  global
        .offset:         16
        .size:           8
        .value_kind:     global_buffer
    .group_segment_fixed_size: 0
    .kernarg_segment_align: 8
    .kernarg_segment_size: 24
    .language:       OpenCL C
    .language_version:
      - 2
      - 0
    .max_flat_workgroup_size: 256
    .name:           _Z7k_finalPKfS0_Pf
    .private_segment_fixed_size: 0
    .sgpr_count:     14
    .sgpr_spill_count: 0
    .symbol:         _Z7k_finalPKfS0_Pf.kd
    .uniform_work_group_size: 1
    .uses_dynamic_stack: false
    .vgpr_count:     11
    .vgpr_spill_count: 0
    .wavefront_size: 64
  - .agpr_count:     0
    .args:
      - .actual_access:  read_only
        .address_space:  global
        .offset:         0
        .size:           8
        .value_kind:     global_buffer
      - .actual_access:  read_only
        .address_space:  global
        .offset:         8
        .size:           8
        .value_kind:     global_buffer
      - .actual_access:  read_only
        .address_space:  global
        .offset:         16
        .size:           8
        .value_kind:     global_buffer
      - .actual_access:  read_only
        .address_space:  global
        .offset:         24
        .size:           8
        .value_kind:     global_buffer
      - .actual_access:  read_only
        .address_space:  global
        .offset:         32
        .size:           8
        .value_kind:     global_buffer
      - .actual_access:  read_only
        .address_space:  global
        .offset:         40
        .size:           8
        .value_kind:     global_buffer
      - .address_space:  global
        .offset:         48
        .size:           8
        .value_kind:     global_buffer
      - .actual_access:  write_only
        .address_space:  global
        .offset:         56
        .size:           8
        .value_kind:     global_buffer
      - .address_space:  global
        .offset:         64
        .size:           8
        .value_kind:     global_buffer
      - .actual_access:  read_only
        .address_space:  global
        .offset:         72
        .size:           8
        .value_kind:     global_buffer
      - .address_space:  global
        .offset:         80
        .size:           8
        .value_kind:     global_buffer
      - .actual_access:  read_only
        .address_space:  global
        .offset:         88
        .size:           8
        .value_kind:     global_buffer
      - .offset:         96
        .size:           4
        .value_kind:     hidden_block_count_x
      - .offset:         100
        .size:           4
        .value_kind:     hidden_block_count_y
      - .offset:         104
        .size:           4
        .value_kind:     hidden_block_count_z
      - .offset:         108
        .size:           2
        .value_kind:     hidden_group_size_x
      - .offset:         110
        .size:           2
        .value_kind:     hidden_group_size_y
      - .offset:         112
        .size:           2
        .value_kind:     hidden_group_size_z
      - .offset:         114
        .size:           2
        .value_kind:     hidden_remainder_x
      - .offset:         116
        .size:           2
        .value_kind:     hidden_remainder_y
      - .offset:         118
        .size:           2
        .value_kind:     hidden_remainder_z
      - .offset:         136
        .size:           8
        .value_kind:     hidden_global_offset_x
      - .offset:         144
        .size:           8
        .value_kind:     hidden_global_offset_y
      - .offset:         152
        .size:           8
        .value_kind:     hidden_global_offset_z
      - .offset:         160
        .size:           2
        .value_kind:     hidden_grid_dims
      - .offset:         216
        .size:           4
        .value_kind:     hidden_dynamic_lds_size
    .group_segment_fixed_size: 35072
    .kernarg_segment_align: 8
    .kernarg_segment_size: 352
    .language:       OpenCL C
    .language_version:
      - 2
      - 0
    .max_flat_workgroup_size: 1024
    .name:           _Z7k_layerILi1EEvPKDF16_PKiPKjS3_S3_S1_PKfPDF16_PhS3_S7_Pf
    .private_segment_fixed_size: 0
    .sgpr_count:     43
    .sgpr_spill_count: 0
    .symbol:         _Z7k_layerILi1EEvPKDF16_PKiPKjS3_S3_S1_PKfPDF16_PhS3_S7_Pf.kd
    .uniform_work_group_size: 1
    .uses_dynamic_stack: false
    .vgpr_count:     117
    .vgpr_spill_count: 0
    .wavefront_size: 64
  - .agpr_count:     0
    .args:
      - .actual_access:  read_only
        .address_space:  global
        .offset:         0
        .size:           8
        .value_kind:     global_buffer
      - .actual_access:  read_only
        .address_space:  global
        .offset:         8
        .size:           8
        .value_kind:     global_buffer
      - .actual_access:  read_only
        .address_space:  global
        .offset:         16
        .size:           8
        .value_kind:     global_buffer
      - .actual_access:  read_only
        .address_space:  global
        .offset:         24
        .size:           8
        .value_kind:     global_buffer
      - .actual_access:  read_only
        .address_space:  global
        .offset:         32
        .size:           8
        .value_kind:     global_buffer
      - .actual_access:  read_only
        .address_space:  global
        .offset:         40
        .size:           8
        .value_kind:     global_buffer
      - .address_space:  global
        .offset:         48
        .size:           8
        .value_kind:     global_buffer
      - .actual_access:  read_only
        .address_space:  global
        .offset:         56
        .size:           8
        .value_kind:     global_buffer
      - .address_space:  global
        .offset:         64
        .size:           8
        .value_kind:     global_buffer
      - .actual_access:  read_only
        .address_space:  global
        .offset:         72
        .size:           8
        .value_kind:     global_buffer
      - .address_space:  global
        .offset:         80
        .size:           8
        .value_kind:     global_buffer
      - .address_space:  global
        .offset:         88
        .size:           8
        .value_kind:     global_buffer
      - .offset:         96
        .size:           4
        .value_kind:     hidden_block_count_x
      - .offset:         100
        .size:           4
        .value_kind:     hidden_block_count_y
      - .offset:         104
        .size:           4
        .value_kind:     hidden_block_count_z
      - .offset:         108
        .size:           2
        .value_kind:     hidden_group_size_x
      - .offset:         110
        .size:           2
        .value_kind:     hidden_group_size_y
      - .offset:         112
        .size:           2
        .value_kind:     hidden_group_size_z
      - .offset:         114
        .size:           2
        .value_kind:     hidden_remainder_x
      - .offset:         116
        .size:           2
        .value_kind:     hidden_remainder_y
      - .offset:         118
        .size:           2
        .value_kind:     hidden_remainder_z
      - .offset:         136
        .size:           8
        .value_kind:     hidden_global_offset_x
      - .offset:         144
        .size:           8
        .value_kind:     hidden_global_offset_y
      - .offset:         152
        .size:           8
        .value_kind:     hidden_global_offset_z
      - .offset:         160
        .size:           2
        .value_kind:     hidden_grid_dims
      - .offset:         216
        .size:           4
        .value_kind:     hidden_dynamic_lds_size
    .group_segment_fixed_size: 35584
    .kernarg_segment_align: 8
    .kernarg_segment_size: 352
    .language:       OpenCL C
    .language_version:
      - 2
      - 0
    .max_flat_workgroup_size: 1024
    .name:           _Z7k_layerILi2EEvPKDF16_PKiPKjS3_S3_S1_PKfPDF16_PhS3_S7_Pf
    .private_segment_fixed_size: 0
    .sgpr_count:     48
    .sgpr_spill_count: 0
    .symbol:         _Z7k_layerILi2EEvPKDF16_PKiPKjS3_S3_S1_PKfPDF16_PhS3_S7_Pf.kd
    .uniform_work_group_size: 1
    .uses_dynamic_stack: false
    .vgpr_count:     105
    .vgpr_spill_count: 0
    .wavefront_size: 64
